# grid barrier release flattened: waiting workgroups poll the cross-XCD generation word directly, leaders no longer bump/wait on the per-XCD release word (arrival protocol and acquire unchanged)
# speedup vs baseline: 1.0107x; 1.0022x over previous
; __device__ __forceinline__ unsigned xb_ld(unsigned* p)              { return __hip_atomic_load(p, __ATOMIC_RELAXED, __HIP_MEMORY_SCOPE_AGENT); }
; __device__ __forceinline__ unsigned xb_add(unsigned* p, unsigned v) { return __hip_atomic_fetch_add(p, v, __ATOMIC_RELAXED, __HIP_MEMORY_SCOPE_AGENT); }
; #define XB_SPIN(cond, bar) do { unsigned _sp = 0; while (cond) { __builtin_amdgcn_s_sleep(1); \
;     if ((++_sp & 255u) == 0u) { if (xb_ld(&(bar)[XB_TMO])) break; if (_sp > XB_SPIN_CAP) { atomicAdd(&(bar)[XB_TMO], 1u); break; } } } } while (0)
; __device__ __forceinline__ void xcd_barrier(const XcdBarrier& b) {
;     ...
;         const unsigned old = xb_add(&bar[XB_XSUB(b.x)], 1u);
;         const unsigned gen = old / nloc;
;         if (old + 1u == (gen + 1u) * nloc) {
;             __builtin_amdgcn_fence(__ATOMIC_RELEASE, "agent");
;             asm volatile("s_waitcnt vmcnt(0)" ::: "memory");
;             const unsigned og = xb_add(&bar[XB_TOP], 1u);
;             const unsigned tg = og / nx;
;             if (og + 1u == (tg + 1u) * nx) xb_add(&bar[XB_TOPGEN], 1u);
;             else XB_SPIN(xb_ld(&bar[XB_TOPGEN]) == tg, bar);
;             __builtin_amdgcn_fence(__ATOMIC_ACQUIRE, "agent");
;             xb_add(&bar[XB_XGEN(b.x)], 1u);
;             asm volatile("s_waitcnt vmcnt(0)" ::: "memory");
;         } else {
;             XB_SPIN(xb_ld(&bar[XB_XGEN(b.x)]) == gen, bar);
;             __builtin_amdgcn_fence(__ATOMIC_ACQUIRE, "agent");
;             asm volatile("s_waitcnt vmcnt(0)" ::: "memory");
;         }
.LBB0_416:
	s_or_b64 exec, exec, s[6:7]
	v_readlane_b32 s4, v254, 19
	v_readlane_b32 s5, v254, 20
	s_waitcnt vmcnt(0)
	buffer_inv sc1
	s_nop 2
	s_waitcnt vmcnt(0)

; __device__ __forceinline__ unsigned xb_ld(unsigned* p)              { return __hip_atomic_load(p, __ATOMIC_RELAXED, __HIP_MEMORY_SCOPE_AGENT); }
; __device__ __forceinline__ unsigned xb_add(unsigned* p, unsigned v) { return __hip_atomic_fetch_add(p, v, __ATOMIC_RELAXED, __HIP_MEMORY_SCOPE_AGENT); }
; #define XB_SPIN(cond, bar) do { unsigned _sp = 0; while (cond) { __builtin_amdgcn_s_sleep(1); \
;     if ((++_sp & 255u) == 0u) { if (xb_ld(&(bar)[XB_TMO])) break; if (_sp > XB_SPIN_CAP) { atomicAdd(&(bar)[XB_TMO], 1u); break; } } } } while (0)
; __device__ __forceinline__ void xcd_barrier(const XcdBarrier& b) {
;     ...
;         const unsigned old = xb_add(&bar[XB_XSUB(b.x)], 1u);
;         const unsigned gen = old / nloc;
;         if (old + 1u == (gen + 1u) * nloc) {
;             __builtin_amdgcn_fence(__ATOMIC_RELEASE, "agent");
;             asm volatile("s_waitcnt vmcnt(0)" ::: "memory");
;             const unsigned og = xb_add(&bar[XB_TOP], 1u);
;             const unsigned tg = og / nx;
;             if (og + 1u == (tg + 1u) * nx) xb_add(&bar[XB_TOPGEN], 1u);
;             else XB_SPIN(xb_ld(&bar[XB_TOPGEN]) == tg, bar);
;             __builtin_amdgcn_fence(__ATOMIC_ACQUIRE, "agent");
;             xb_add(&bar[XB_XGEN(b.x)], 1u);
;             asm volatile("s_waitcnt vmcnt(0)" ::: "memory");
;         } else {
;             XB_SPIN(xb_ld(&bar[XB_XGEN(b.x)]) == gen, bar);
.LBB0_455:
	v_readlane_b32 s4, v254, 17
	v_readlane_b32 s5, v254, 18
	v_cvt_f32_u32_e32 v1, v4
	v_sub_u32_e32 v6, 0, v4
	v_rcp_iflag_f32_e32 v1, v1
	s_nop 1
	global_atomic_add v5, v3, v244, s[4:5] sc0
	v_mul_f32_e32 v1, 0x4f7ffffe, v1
	v_cvt_u32_f32_e32 v1, v1
	v_mul_lo_u32 v6, v6, v1
	v_mul_hi_u32 v6, v1, v6
	v_add_u32_e32 v1, v1, v6
	s_waitcnt vmcnt(0)
	v_mul_hi_u32 v1, v5, v1
	v_mul_lo_u32 v6, v1, v4
	v_sub_u32_e32 v6, v5, v6
	v_add_u32_e32 v7, 1, v1
	v_cmp_ge_u32_e32 vcc, v6, v4
	v_add_u32_e32 v5, 1, v5
	s_nop 0
	v_cndmask_b32_e32 v1, v1, v7, vcc
	v_sub_u32_e32 v7, v6, v4
	v_cndmask_b32_e32 v6, v6, v7, vcc
	v_add_u32_e32 v7, 1, v1
	v_cmp_ge_u32_e32 vcc, v6, v4
	s_nop 1
	v_cndmask_b32_e32 v1, v1, v7, vcc
	v_mul_lo_u32 v6, v4, v1
	v_add_u32_e32 v4, v6, v4
	v_cmp_ne_u32_e32 vcc, v5, v4
	s_and_saveexec_b64 s[4:5], vcc
	s_xor_b64 s[44:45], exec, s[4:5]
	s_cbranch_execz .LBB0_469
	v_readlane_b32 s4, v254, 23
	v_readlane_b32 s5, v254, 24
	s_waitcnt lgkmcnt(0)
	s_nop 3
	global_load_dword v2, v3, s[4:5] sc1
	s_waitcnt vmcnt(0)
	v_cmp_eq_u32_e32 vcc, v2, v1
	s_and_saveexec_b64 s[48:49], vcc
	s_cbranch_execz .LBB0_468
	s_mov_b32 s18, 1
	s_mov_b64 s[4:5], 0
	s_branch .LBB0_459

; __device__ __forceinline__ unsigned xb_ld(unsigned* p)              { return __hip_atomic_load(p, __ATOMIC_RELAXED, __HIP_MEMORY_SCOPE_AGENT); }
; __device__ __forceinline__ unsigned xb_add(unsigned* p, unsigned v) { return __hip_atomic_fetch_add(p, v, __ATOMIC_RELAXED, __HIP_MEMORY_SCOPE_AGENT); }
; #define XB_SPIN(cond, bar) do { unsigned _sp = 0; while (cond) { __builtin_amdgcn_s_sleep(1); \
;     if ((++_sp & 255u) == 0u) { if (xb_ld(&(bar)[XB_TMO])) break; if (_sp > XB_SPIN_CAP) { atomicAdd(&(bar)[XB_TMO], 1u); break; } } } } while (0)
; __device__ __forceinline__ void xcd_barrier(const XcdBarrier& b) {
;     ...
;         const unsigned old = xb_add(&bar[XB_XSUB(b.x)], 1u);
;         const unsigned gen = old / nloc;
;         if (old + 1u == (gen + 1u) * nloc) {
;             __builtin_amdgcn_fence(__ATOMIC_RELEASE, "agent");
;             asm volatile("s_waitcnt vmcnt(0)" ::: "memory");
;             const unsigned og = xb_add(&bar[XB_TOP], 1u);
;             const unsigned tg = og / nx;
;             if (og + 1u == (tg + 1u) * nx) xb_add(&bar[XB_TOPGEN], 1u);
;             else XB_SPIN(xb_ld(&bar[XB_TOPGEN]) == tg, bar);
;             __builtin_amdgcn_fence(__ATOMIC_ACQUIRE, "agent");
;             xb_add(&bar[XB_XGEN(b.x)], 1u);
;             asm volatile("s_waitcnt vmcnt(0)" ::: "memory");
;         } else {
;             XB_SPIN(xb_ld(&bar[XB_XGEN(b.x)]) == gen, bar);
.LBB0_548:
	v_readlane_b32 s4, v254, 17
	v_readlane_b32 s5, v254, 18
	v_cvt_f32_u32_e32 v1, v4
	v_sub_u32_e32 v6, 0, v4
	v_rcp_iflag_f32_e32 v1, v1
	s_nop 1
	global_atomic_add v5, v3, v244, s[4:5] sc0
	v_mul_f32_e32 v1, 0x4f7ffffe, v1
	v_cvt_u32_f32_e32 v1, v1
	v_mul_lo_u32 v6, v6, v1
	v_mul_hi_u32 v6, v1, v6
	v_add_u32_e32 v1, v1, v6
	s_waitcnt vmcnt(0)
	v_mul_hi_u32 v1, v5, v1
	v_mul_lo_u32 v6, v1, v4
	v_sub_u32_e32 v6, v5, v6
	v_add_u32_e32 v7, 1, v1
	v_cmp_ge_u32_e32 vcc, v6, v4
	v_add_u32_e32 v5, 1, v5
	s_nop 0
	v_cndmask_b32_e32 v1, v1, v7, vcc
	v_sub_u32_e32 v7, v6, v4
	v_cndmask_b32_e32 v6, v6, v7, vcc
	v_add_u32_e32 v7, 1, v1
	v_cmp_ge_u32_e32 vcc, v6, v4
	s_nop 1
	v_cndmask_b32_e32 v1, v1, v7, vcc
	v_mul_lo_u32 v6, v4, v1
	v_add_u32_e32 v4, v6, v4
	v_cmp_ne_u32_e32 vcc, v5, v4
	s_and_saveexec_b64 s[4:5], vcc
	s_xor_b64 s[40:41], exec, s[4:5]
	s_cbranch_execz .LBB0_562
	v_readlane_b32 s4, v254, 23
	v_readlane_b32 s5, v254, 24
	s_waitcnt lgkmcnt(0)
	s_nop 3
	global_load_dword v2, v3, s[4:5] sc1
	s_waitcnt vmcnt(0)
	v_cmp_eq_u32_e32 vcc, v2, v1
	s_and_saveexec_b64 s[42:43], vcc
	s_cbranch_execz .LBB0_561
	s_mov_b32 s18, 1
	s_mov_b64 s[4:5], 0
	s_branch .LBB0_552

; __device__ __forceinline__ unsigned xb_ld(unsigned* p)              { return __hip_atomic_load(p, __ATOMIC_RELAXED, __HIP_MEMORY_SCOPE_AGENT); }
; __device__ __forceinline__ unsigned xb_add(unsigned* p, unsigned v) { return __hip_atomic_fetch_add(p, v, __ATOMIC_RELAXED, __HIP_MEMORY_SCOPE_AGENT); }
; #define XB_SPIN(cond, bar) do { unsigned _sp = 0; while (cond) { __builtin_amdgcn_s_sleep(1); \
;     if ((++_sp & 255u) == 0u) { if (xb_ld(&(bar)[XB_TMO])) break; if (_sp > XB_SPIN_CAP) { atomicAdd(&(bar)[XB_TMO], 1u); break; } } } } while (0)
; __device__ __forceinline__ void xcd_barrier(const XcdBarrier& b) {
;     ...
;         const unsigned old = xb_add(&bar[XB_XSUB(b.x)], 1u);
;         const unsigned gen = old / nloc;
;         if (old + 1u == (gen + 1u) * nloc) {
;             __builtin_amdgcn_fence(__ATOMIC_RELEASE, "agent");
;             asm volatile("s_waitcnt vmcnt(0)" ::: "memory");
;             const unsigned og = xb_add(&bar[XB_TOP], 1u);
;             const unsigned tg = og / nx;
;             if (og + 1u == (tg + 1u) * nx) xb_add(&bar[XB_TOPGEN], 1u);
;             else XB_SPIN(xb_ld(&bar[XB_TOPGEN]) == tg, bar);
;             __builtin_amdgcn_fence(__ATOMIC_ACQUIRE, "agent");
;             xb_add(&bar[XB_XGEN(b.x)], 1u);
;             asm volatile("s_waitcnt vmcnt(0)" ::: "memory");
;         } else {
;             XB_SPIN(xb_ld(&bar[XB_XGEN(b.x)]) == gen, bar);
.LBB0_1538:
	v_readlane_b32 s4, v254, 17
	v_readlane_b32 s5, v254, 18
	v_cvt_f32_u32_e32 v1, v4
	v_sub_u32_e32 v6, 0, v4
	v_rcp_iflag_f32_e32 v1, v1
	s_nop 1
	global_atomic_add v5, v3, v244, s[4:5] sc0
	v_mul_f32_e32 v1, 0x4f7ffffe, v1
	v_cvt_u32_f32_e32 v1, v1
	v_mul_lo_u32 v6, v6, v1
	v_mul_hi_u32 v6, v1, v6
	v_add_u32_e32 v1, v1, v6
	s_waitcnt vmcnt(0)
	v_mul_hi_u32 v1, v5, v1
	v_mul_lo_u32 v6, v1, v4
	v_sub_u32_e32 v6, v5, v6
	v_add_u32_e32 v7, 1, v1
	v_cmp_ge_u32_e32 vcc, v6, v4
	v_add_u32_e32 v5, 1, v5
	s_nop 0
	v_cndmask_b32_e32 v1, v1, v7, vcc
	v_sub_u32_e32 v7, v6, v4
	v_cndmask_b32_e32 v6, v6, v7, vcc
	v_add_u32_e32 v7, 1, v1
	v_cmp_ge_u32_e32 vcc, v6, v4
	s_nop 1
	v_cndmask_b32_e32 v1, v1, v7, vcc
	v_mul_lo_u32 v6, v4, v1
	v_add_u32_e32 v4, v6, v4
	v_cmp_ne_u32_e32 vcc, v5, v4
	s_and_saveexec_b64 s[4:5], vcc
	s_xor_b64 s[40:41], exec, s[4:5]
	s_cbranch_execz .LBB0_1552
	v_readlane_b32 s4, v254, 23
	v_readlane_b32 s5, v254, 24
	s_waitcnt lgkmcnt(0)
	s_nop 3
	global_load_dword v2, v3, s[4:5] sc1
	s_waitcnt vmcnt(0)
	v_cmp_eq_u32_e32 vcc, v2, v1
	s_and_saveexec_b64 s[42:43], vcc
	s_cbranch_execz .LBB0_1551
	s_mov_b32 s17, 1
	s_mov_b64 s[4:5], 0
	s_branch .LBB0_1542

; __device__ __forceinline__ unsigned xb_ld(unsigned* p)              { return __hip_atomic_load(p, __ATOMIC_RELAXED, __HIP_MEMORY_SCOPE_AGENT); }
; __device__ __forceinline__ unsigned xb_add(unsigned* p, unsigned v) { return __hip_atomic_fetch_add(p, v, __ATOMIC_RELAXED, __HIP_MEMORY_SCOPE_AGENT); }
; #define XB_SPIN(cond, bar) do { unsigned _sp = 0; while (cond) { __builtin_amdgcn_s_sleep(1); \
;     if ((++_sp & 255u) == 0u) { if (xb_ld(&(bar)[XB_TMO])) break; if (_sp > XB_SPIN_CAP) { atomicAdd(&(bar)[XB_TMO], 1u); break; } } } } while (0)
; __device__ __forceinline__ void xcd_barrier(const XcdBarrier& b) {
;     ...
;         const unsigned old = xb_add(&bar[XB_XSUB(b.x)], 1u);
;         const unsigned gen = old / nloc;
;         if (old + 1u == (gen + 1u) * nloc) {
;             __builtin_amdgcn_fence(__ATOMIC_RELEASE, "agent");
;             asm volatile("s_waitcnt vmcnt(0)" ::: "memory");
;             const unsigned og = xb_add(&bar[XB_TOP], 1u);
;             const unsigned tg = og / nx;
;             if (og + 1u == (tg + 1u) * nx) xb_add(&bar[XB_TOPGEN], 1u);
;             else XB_SPIN(xb_ld(&bar[XB_TOPGEN]) == tg, bar);
;             __builtin_amdgcn_fence(__ATOMIC_ACQUIRE, "agent");
;             xb_add(&bar[XB_XGEN(b.x)], 1u);
;             asm volatile("s_waitcnt vmcnt(0)" ::: "memory");
;         } else {
;             XB_SPIN(xb_ld(&bar[XB_XGEN(b.x)]) == gen, bar);
.LBB0_1761:
	v_readlane_b32 s4, v254, 17
	v_readlane_b32 s5, v254, 18
	v_cvt_f32_u32_e32 v1, v4
	v_sub_u32_e32 v6, 0, v4
	v_rcp_iflag_f32_e32 v1, v1
	s_nop 1
	global_atomic_add v5, v3, v244, s[4:5] sc0
	v_mul_f32_e32 v1, 0x4f7ffffe, v1
	v_cvt_u32_f32_e32 v1, v1
	v_mul_lo_u32 v6, v6, v1
	v_mul_hi_u32 v6, v1, v6
	v_add_u32_e32 v1, v1, v6
	s_waitcnt vmcnt(0)
	v_mul_hi_u32 v1, v5, v1
	v_mul_lo_u32 v6, v1, v4
	v_sub_u32_e32 v6, v5, v6
	v_add_u32_e32 v7, 1, v1
	v_cmp_ge_u32_e32 vcc, v6, v4
	v_add_u32_e32 v5, 1, v5
	s_nop 0
	v_cndmask_b32_e32 v1, v1, v7, vcc
	v_sub_u32_e32 v7, v6, v4
	v_cndmask_b32_e32 v6, v6, v7, vcc
	v_add_u32_e32 v7, 1, v1
	v_cmp_ge_u32_e32 vcc, v6, v4
	s_nop 1
	v_cndmask_b32_e32 v1, v1, v7, vcc
	v_mul_lo_u32 v6, v4, v1
	v_add_u32_e32 v4, v6, v4
	v_cmp_ne_u32_e32 vcc, v5, v4
	s_and_saveexec_b64 s[4:5], vcc
	s_xor_b64 s[44:45], exec, s[4:5]
	s_cbranch_execz .LBB0_1792
	v_readlane_b32 s4, v254, 23
	v_readlane_b32 s5, v254, 24
	s_waitcnt lgkmcnt(0)
	s_nop 3
	global_load_dword v2, v3, s[4:5] sc1
	s_waitcnt vmcnt(0)
	v_cmp_eq_u32_e32 vcc, v2, v1
	s_and_saveexec_b64 s[46:47], vcc
	s_cbranch_execz .LBB0_1791
	s_mov_b32 s17, 1
	s_mov_b64 s[4:5], 0
	s_branch .LBB0_1765
